# stack: memkv move, mlstm_c q prefetch, mlstm_a prefetch, gates wait fix, out-proj residual prefetch
# baseline (speedup 1.0000x reference)
.Lgates_418b:
	s_waitcnt vmcnt(9)
	v_mfma_f32_16x16x32_bf16 v[38:41], v[38:41], v[34:37], v[50:53]
	s_add_i32 s9, s9, 2
	v_lshl_add_u64 v[66:67], v[66:67], 0, s[18:19]
	s_andn2_b64 vcc, exec, s[20:21]
	s_waitcnt vmcnt(8)
	v_mfma_f32_16x16x32_bf16 v[38:41], v[42:45], v[30:33], v[38:41]
	s_waitcnt vmcnt(7)
	v_mfma_f32_16x16x32_bf16 v[34:37], v[46:49], v[34:37], v[38:41]
	s_waitcnt vmcnt(6)
	v_mfma_f32_16x16x32_bf16 v[26:29], v[26:29], v[30:33], v[34:37]
	s_cbranch_vccz .LBB0_421
	s_branch .LBB0_419

.LBB0_772:
	v_mov_b32_e32 v132, v0
	s_ashr_i32 s41, s40, 31
	v_ashrrev_i32_e32 v130, 2, v132
	v_and_b32_e32 v130, 0xffffffc0, v130
	s_lshl_b64 s[40:41], s[40:41], 8
	v_ashrrev_i32_e32 v131, 31, v130
	v_lshl_add_u64 v[130:131], s[40:41], 0, v[130:131]
	v_and_or_b32 v130, v132, 31, v130
	s_lshl_b32 s31, s64, 8
	v_lshrrev_b32_e32 v132, 1, v132
	s_ashr_i32 s35, s31, 31
	v_and_b32_e32 v133, 0x60, v132
	v_and_b32_e32 v132, 16, v132
	v_or3_b32 v132, s31, v133, v132
	v_mov_b32_e32 v133, s35
	v_lshlrev_b64 v[130:131], 11, v[130:131]
	v_lshl_add_u64 v[130:131], v[130:131], 0, v[132:133]
	v_lshlrev_b64 v[130:131], 1, v[130:131]
	v_lshl_add_u64 v[156:157], s[10:11], 0, v[130:131]
	global_load_dwordx4 v[174:177], v[156:157], off
	global_load_dwordx4 v[178:181], v[156:157], off offset:16
	global_load_dwordx4 v[182:185], v[156:157], off offset:256
	global_load_dwordx4 v[186:189], v[156:157], off offset:272
	v_add_co_u32_e32 v132, vcc, s61, v156
	v_lshl_add_u64 v[154:155], s[12:13], 0, v[130:131]
	s_nop 0
	v_addc_co_u32_e32 v133, vcc, 0, v157, vcc
	global_load_dwordx4 v[190:193], v[132:133], off
	v_lshl_add_u64 v[130:131], v[156:157], 0, s[18:19]
	v_lshl_add_u64 v[198:199], v[156:157], 0, s[20:21]
	global_load_dwordx4 v[194:197], v[130:131], off offset:16
	global_load_dwordx4 v[134:137], v[132:133], off offset:256
	s_nop 0
	global_load_dwordx4 v[130:133], v[198:199], off offset:16
	v_add_co_u32_e32 v214, vcc, s62, v156
	v_lshl_add_u64 v[216:217], v[156:157], 0, s[26:27]
	s_nop 0
	v_addc_co_u32_e32 v215, vcc, 0, v157, vcc
	global_load_dwordx4 v[218:221], v[214:215], off
	v_lshl_add_u64 v[214:215], v[156:157], 0, s[24:25]
	global_load_dwordx4 v[222:225], v[214:215], off offset:16
	global_load_dwordx4 v[226:229], v[214:215], off offset:256
	global_load_dwordx4 v[230:233], v[214:215], off offset:272
	v_add_co_u32_e32 v214, vcc, s63, v156
	global_load_dwordx4 v[240:243], v[216:217], off offset:16
	s_nop 0
	v_addc_co_u32_e32 v215, vcc, 0, v157, vcc
	global_load_dwordx4 v[236:239], v[214:215], off
	v_lshl_add_u64 v[216:217], v[156:157], 0, s[28:29]
	global_load_dwordx4 v[248:251], v[214:215], off offset:256
	s_nop 0
	global_load_dwordx4 v[214:217], v[216:217], off offset:16
	s_waitcnt vmcnt(8)
	v_lshlrev_b32_e32 v198, 16, v174
	v_and_b32_e32 v199, 0xffff0000, v174
	v_lshlrev_b32_e32 v174, 16, v175
	v_and_b32_e32 v175, 0xffff0000, v175
	v_lshlrev_b32_e32 v200, 16, v176
	v_and_b32_e32 v201, 0xffff0000, v176
	v_lshlrev_b32_e32 v176, 16, v177
	v_and_b32_e32 v177, 0xffff0000, v177
	v_lshlrev_b32_e32 v202, 16, v178
	v_and_b32_e32 v203, 0xffff0000, v178
	v_lshlrev_b32_e32 v178, 16, v179
	v_and_b32_e32 v179, 0xffff0000, v179
	v_lshlrev_b32_e32 v204, 16, v180
	v_and_b32_e32 v205, 0xffff0000, v180
	v_lshlrev_b32_e32 v180, 16, v181
	v_and_b32_e32 v181, 0xffff0000, v181
	v_lshlrev_b32_e32 v206, 16, v182
	v_and_b32_e32 v207, 0xffff0000, v182
	v_lshlrev_b32_e32 v182, 16, v183
	v_and_b32_e32 v183, 0xffff0000, v183
	v_lshlrev_b32_e32 v208, 16, v184
	v_and_b32_e32 v209, 0xffff0000, v184
	v_lshlrev_b32_e32 v184, 16, v185
	v_and_b32_e32 v185, 0xffff0000, v185
	v_pk_fma_f32 v[114:115], v[114:115], s[22:23], v[198:199] op_sel_hi:[1,0,1]
	v_pk_fma_f32 v[116:117], v[116:117], s[22:23], v[174:175] op_sel_hi:[1,0,1]
	v_pk_fma_f32 v[118:119], v[118:119], s[22:23], v[200:201] op_sel_hi:[1,0,1]
	v_pk_fma_f32 v[120:121], v[120:121], s[22:23], v[176:177] op_sel_hi:[1,0,1]
	v_lshlrev_b32_e32 v210, 16, v186
	v_and_b32_e32 v211, 0xffff0000, v186
	v_lshlrev_b32_e32 v186, 16, v187
	v_and_b32_e32 v187, 0xffff0000, v187
	v_lshlrev_b32_e32 v212, 16, v188
	v_pk_fma_f32 v[122:123], v[122:123], s[22:23], v[202:203] op_sel_hi:[1,0,1]
	v_pk_fma_f32 v[124:125], v[124:125], s[22:23], v[178:179] op_sel_hi:[1,0,1]
	v_pk_fma_f32 v[126:127], v[126:127], s[22:23], v[204:205] op_sel_hi:[1,0,1]
	v_pk_fma_f32 v[128:129], v[128:129], s[22:23], v[180:181] op_sel_hi:[1,0,1]
	v_pk_fma_f32 v[174:175], v[98:99], s[22:23], v[206:207] op_sel_hi:[1,0,1]
	v_pk_fma_f32 v[176:177], v[100:101], s[22:23], v[182:183] op_sel_hi:[1,0,1]
	v_pk_fma_f32 v[178:179], v[102:103], s[22:23], v[208:209] op_sel_hi:[1,0,1]
	v_pk_fma_f32 v[180:181], v[104:105], s[22:23], v[184:185] op_sel_hi:[1,0,1]
	v_cvt_pk_bf16_f32 v98, v114, v115
	v_cvt_pk_bf16_f32 v99, v116, v117
	v_cvt_pk_bf16_f32 v100, v118, v119
	v_cvt_pk_bf16_f32 v101, v120, v121
	v_and_b32_e32 v213, 0xffff0000, v188
	v_pk_fma_f32 v[182:183], v[106:107], s[22:23], v[210:211] op_sel_hi:[1,0,1]
	v_pk_fma_f32 v[184:185], v[108:109], s[22:23], v[186:187] op_sel_hi:[1,0,1]
	v_cvt_pk_bf16_f32 v102, v122, v123
	v_cvt_pk_bf16_f32 v103, v124, v125
	v_cvt_pk_bf16_f32 v104, v126, v127
	v_cvt_pk_bf16_f32 v105, v128, v129
	v_cvt_pk_bf16_f32 v106, v174, v175
	v_cvt_pk_bf16_f32 v107, v176, v177
	v_cvt_pk_bf16_f32 v108, v178, v179
	v_cvt_pk_bf16_f32 v109, v180, v181
	global_store_dwordx4 v[154:155], v[98:101], off
	global_store_dwordx4 v[154:155], v[102:105], off offset:16
	global_store_dwordx4 v[154:155], v[106:109], off offset:256
	v_pk_fma_f32 v[98:99], v[110:111], s[22:23], v[212:213] op_sel_hi:[1,0,1]
	v_cvt_pk_bf16_f32 v114, v182, v183
	v_cvt_pk_bf16_f32 v116, v98, v99
	v_lshlrev_b32_e32 v98, 16, v189
	v_and_b32_e32 v99, 0xffff0000, v189
	v_pk_fma_f32 v[98:99], v[112:113], s[22:23], v[98:99] op_sel_hi:[1,0,1]
	v_cvt_pk_bf16_f32 v115, v184, v185
	v_cvt_pk_bf16_f32 v117, v98, v99
	v_lshlrev_b32_e32 v98, 16, v190
	v_and_b32_e32 v99, 0xffff0000, v190
	v_pk_fma_f32 v[82:83], v[82:83], s[22:23], v[98:99] op_sel_hi:[1,0,1]
	v_lshlrev_b32_e32 v98, 16, v191
	v_and_b32_e32 v99, 0xffff0000, v191
	v_pk_fma_f32 v[84:85], v[84:85], s[22:23], v[98:99] op_sel_hi:[1,0,1]
	v_cvt_pk_bf16_f32 v82, v82, v83
	v_cvt_pk_bf16_f32 v83, v84, v85
	v_lshlrev_b32_e32 v84, 16, v192
	v_and_b32_e32 v85, 0xffff0000, v192
	v_pk_fma_f32 v[84:85], v[86:87], s[22:23], v[84:85] op_sel_hi:[1,0,1]
	v_lshlrev_b32_e32 v86, 16, v193
	v_and_b32_e32 v87, 0xffff0000, v193
	v_pk_fma_f32 v[86:87], v[88:89], s[22:23], v[86:87] op_sel_hi:[1,0,1]
	v_cvt_pk_bf16_f32 v84, v84, v85
	v_cvt_pk_bf16_f32 v85, v86, v87
	v_add_co_u32_e32 v86, vcc, s61, v154
	v_lshlrev_b32_e32 v88, 16, v197
	s_nop 0
	v_addc_co_u32_e32 v87, vcc, 0, v155, vcc
	global_store_dwordx4 v[86:87], v[82:85], off
	v_and_b32_e32 v89, 0xffff0000, v197
	v_pk_fma_f32 v[88:89], v[96:97], s[22:23], v[88:89] op_sel_hi:[1,0,1]
	v_lshlrev_b32_e32 v82, 16, v194
	v_and_b32_e32 v83, 0xffff0000, v194
	v_lshlrev_b32_e32 v84, 16, v195
	v_and_b32_e32 v85, 0xffff0000, v195
	v_pk_fma_f32 v[82:83], v[90:91], s[22:23], v[82:83] op_sel_hi:[1,0,1]
	v_pk_fma_f32 v[84:85], v[92:93], s[22:23], v[84:85] op_sel_hi:[1,0,1]
	v_cvt_pk_bf16_f32 v82, v82, v83
	v_cvt_pk_bf16_f32 v83, v84, v85
	v_lshlrev_b32_e32 v84, 16, v196
	v_and_b32_e32 v85, 0xffff0000, v196
	v_pk_fma_f32 v[84:85], v[94:95], s[22:23], v[84:85] op_sel_hi:[1,0,1]
	global_store_dwordx4 v[154:155], v[114:117], off offset:272
	v_cvt_pk_bf16_f32 v84, v84, v85
	v_cvt_pk_bf16_f32 v85, v88, v89
	global_store_dwordx4 v[86:87], v[82:85], off offset:16
	v_lshl_add_u64 v[98:99], v[154:155], 0, s[24:25]
	s_nop 0
	v_lshlrev_b32_e32 v82, 16, v134
	v_and_b32_e32 v83, 0xffff0000, v134
	v_pk_fma_f32 v[66:67], v[66:67], s[22:23], v[82:83] op_sel_hi:[1,0,1]
	v_lshlrev_b32_e32 v82, 16, v135
	v_and_b32_e32 v83, 0xffff0000, v135
	v_pk_fma_f32 v[68:69], v[68:69], s[22:23], v[82:83] op_sel_hi:[1,0,1]
	v_cvt_pk_bf16_f32 v66, v66, v67
	v_cvt_pk_bf16_f32 v67, v68, v69
	v_lshlrev_b32_e32 v68, 16, v136
	v_and_b32_e32 v69, 0xffff0000, v136
	v_pk_fma_f32 v[68:69], v[70:71], s[22:23], v[68:69] op_sel_hi:[1,0,1]
	v_lshlrev_b32_e32 v70, 16, v137
	v_and_b32_e32 v71, 0xffff0000, v137
	v_pk_fma_f32 v[70:71], v[72:73], s[22:23], v[70:71] op_sel_hi:[1,0,1]
	v_cvt_pk_bf16_f32 v68, v68, v69
	v_cvt_pk_bf16_f32 v69, v70, v71
	global_store_dwordx4 v[86:87], v[66:69], off offset:256
	v_lshlrev_b32_e32 v70, 16, v133
	v_and_b32_e32 v71, 0xffff0000, v133
	v_lshlrev_b32_e32 v66, 16, v130
	v_and_b32_e32 v67, 0xffff0000, v130
	v_lshlrev_b32_e32 v68, 16, v131
	v_and_b32_e32 v69, 0xffff0000, v131
	v_pk_fma_f32 v[66:67], v[74:75], s[22:23], v[66:67] op_sel_hi:[1,0,1]
	v_pk_fma_f32 v[68:69], v[76:77], s[22:23], v[68:69] op_sel_hi:[1,0,1]
	v_cvt_pk_bf16_f32 v66, v66, v67
	v_cvt_pk_bf16_f32 v67, v68, v69
	v_lshlrev_b32_e32 v68, 16, v132
	v_and_b32_e32 v69, 0xffff0000, v132
	v_pk_fma_f32 v[68:69], v[78:79], s[22:23], v[68:69] op_sel_hi:[1,0,1]
	v_pk_fma_f32 v[70:71], v[80:81], s[22:23], v[70:71] op_sel_hi:[1,0,1]
	v_cvt_pk_bf16_f32 v68, v68, v69
	v_cvt_pk_bf16_f32 v69, v70, v71
	global_store_dwordx4 v[86:87], v[66:69], off offset:272
	s_nop 1
	s_waitcnt vmcnt(15)
	v_lshlrev_b32_e32 v100, 16, v218
	v_and_b32_e32 v101, 0xffff0000, v218
	v_lshlrev_b32_e32 v218, 16, v219
	v_and_b32_e32 v219, 0xffff0000, v219
	v_pk_fma_f32 v[50:51], v[50:51], s[22:23], v[100:101] op_sel_hi:[1,0,1]
	v_pk_fma_f32 v[52:53], v[52:53], s[22:23], v[218:219] op_sel_hi:[1,0,1]
	v_cvt_pk_bf16_f32 v50, v50, v51
	v_cvt_pk_bf16_f32 v51, v52, v53
	v_lshlrev_b32_e32 v52, 16, v220
	v_and_b32_e32 v53, 0xffff0000, v220
	v_pk_fma_f32 v[52:53], v[54:55], s[22:23], v[52:53] op_sel_hi:[1,0,1]
	v_lshlrev_b32_e32 v54, 16, v221
	v_and_b32_e32 v55, 0xffff0000, v221
	v_pk_fma_f32 v[54:55], v[56:57], s[22:23], v[54:55] op_sel_hi:[1,0,1]
	v_cvt_pk_bf16_f32 v52, v52, v53
	v_cvt_pk_bf16_f32 v53, v54, v55
	v_add_co_u32_e32 v54, vcc, s62, v154
	s_nop 1
	v_addc_co_u32_e32 v55, vcc, 0, v155, vcc
	global_store_dwordx4 v[54:55], v[50:53], off
	s_waitcnt vmcnt(15)
	v_lshlrev_b32_e32 v54, 16, v225
	v_and_b32_e32 v55, 0xffff0000, v225
	v_lshlrev_b32_e32 v50, 16, v222
	v_and_b32_e32 v51, 0xffff0000, v222
	v_lshlrev_b32_e32 v52, 16, v223
	v_and_b32_e32 v53, 0xffff0000, v223
	v_pk_fma_f32 v[50:51], v[58:59], s[22:23], v[50:51] op_sel_hi:[1,0,1]
	v_pk_fma_f32 v[52:53], v[60:61], s[22:23], v[52:53] op_sel_hi:[1,0,1]
	v_cvt_pk_bf16_f32 v50, v50, v51
	v_cvt_pk_bf16_f32 v51, v52, v53
	v_lshlrev_b32_e32 v52, 16, v224
	v_and_b32_e32 v53, 0xffff0000, v224
	v_pk_fma_f32 v[52:53], v[62:63], s[22:23], v[52:53] op_sel_hi:[1,0,1]
	v_pk_fma_f32 v[54:55], v[64:65], s[22:23], v[54:55] op_sel_hi:[1,0,1]
	v_cvt_pk_bf16_f32 v52, v52, v53
	v_cvt_pk_bf16_f32 v53, v54, v55
	global_store_dwordx4 v[98:99], v[50:53], off offset:16
	s_waitcnt vmcnt(15)
	s_nop 0
	v_lshlrev_b32_e32 v50, 16, v226
	v_and_b32_e32 v51, 0xffff0000, v226
	v_pk_fma_f32 v[34:35], v[34:35], s[22:23], v[50:51] op_sel_hi:[1,0,1]
	v_lshlrev_b32_e32 v50, 16, v227
	v_and_b32_e32 v51, 0xffff0000, v227
	v_pk_fma_f32 v[36:37], v[36:37], s[22:23], v[50:51] op_sel_hi:[1,0,1]
	v_cvt_pk_bf16_f32 v34, v34, v35
	v_cvt_pk_bf16_f32 v35, v36, v37
	v_lshlrev_b32_e32 v36, 16, v228
	v_and_b32_e32 v37, 0xffff0000, v228
	v_pk_fma_f32 v[36:37], v[38:39], s[22:23], v[36:37] op_sel_hi:[1,0,1]
	v_lshlrev_b32_e32 v38, 16, v229
	v_and_b32_e32 v39, 0xffff0000, v229
	v_pk_fma_f32 v[38:39], v[40:41], s[22:23], v[38:39] op_sel_hi:[1,0,1]
	v_cvt_pk_bf16_f32 v36, v36, v37
	v_cvt_pk_bf16_f32 v37, v38, v39
	global_store_dwordx4 v[98:99], v[34:37], off offset:256
	s_waitcnt vmcnt(15)
	v_lshlrev_b32_e32 v38, 16, v233
	v_and_b32_e32 v39, 0xffff0000, v233
	v_lshlrev_b32_e32 v34, 16, v230
	v_and_b32_e32 v35, 0xffff0000, v230
	v_lshlrev_b32_e32 v36, 16, v231
	v_and_b32_e32 v37, 0xffff0000, v231
	v_pk_fma_f32 v[34:35], v[42:43], s[22:23], v[34:35] op_sel_hi:[1,0,1]
	v_pk_fma_f32 v[36:37], v[44:45], s[22:23], v[36:37] op_sel_hi:[1,0,1]
	v_cvt_pk_bf16_f32 v34, v34, v35
	v_cvt_pk_bf16_f32 v35, v36, v37
	v_lshlrev_b32_e32 v36, 16, v232
	v_and_b32_e32 v37, 0xffff0000, v232
	v_pk_fma_f32 v[36:37], v[46:47], s[22:23], v[36:37] op_sel_hi:[1,0,1]
	v_pk_fma_f32 v[38:39], v[48:49], s[22:23], v[38:39] op_sel_hi:[1,0,1]
	v_cvt_pk_bf16_f32 v36, v36, v37
	v_cvt_pk_bf16_f32 v37, v38, v39
	global_store_dwordx4 v[98:99], v[34:37], off offset:272
	s_waitcnt vmcnt(14)
	s_nop 0
	v_lshlrev_b32_e32 v34, 16, v236
	v_and_b32_e32 v35, 0xffff0000, v236
	v_pk_fma_f32 v[18:19], v[18:19], s[22:23], v[34:35] op_sel_hi:[1,0,1]
	v_lshlrev_b32_e32 v34, 16, v237
	v_and_b32_e32 v35, 0xffff0000, v237
	v_pk_fma_f32 v[20:21], v[20:21], s[22:23], v[34:35] op_sel_hi:[1,0,1]
	v_cvt_pk_bf16_f32 v18, v18, v19
	v_cvt_pk_bf16_f32 v19, v20, v21
	v_lshlrev_b32_e32 v20, 16, v238
	v_and_b32_e32 v21, 0xffff0000, v238
	v_pk_fma_f32 v[20:21], v[22:23], s[22:23], v[20:21] op_sel_hi:[1,0,1]
	v_lshlrev_b32_e32 v22, 16, v239
	v_and_b32_e32 v23, 0xffff0000, v239
	v_pk_fma_f32 v[22:23], v[24:25], s[22:23], v[22:23] op_sel_hi:[1,0,1]
	v_cvt_pk_bf16_f32 v20, v20, v21
	v_cvt_pk_bf16_f32 v21, v22, v23
	v_add_co_u32_e32 v22, vcc, s63, v154
	v_lshlrev_b32_e32 v24, 16, v243
	s_nop 0
	v_addc_co_u32_e32 v23, vcc, 0, v155, vcc
	global_store_dwordx4 v[22:23], v[18:21], off
	v_and_b32_e32 v25, 0xffff0000, v243
	v_pk_fma_f32 v[24:25], v[32:33], s[22:23], v[24:25] op_sel_hi:[1,0,1]
	v_lshlrev_b32_e32 v18, 16, v240
	v_and_b32_e32 v19, 0xffff0000, v240
	v_lshlrev_b32_e32 v20, 16, v241
	v_and_b32_e32 v21, 0xffff0000, v241
	v_pk_fma_f32 v[18:19], v[26:27], s[22:23], v[18:19] op_sel_hi:[1,0,1]
	v_pk_fma_f32 v[20:21], v[28:29], s[22:23], v[20:21] op_sel_hi:[1,0,1]
	v_cvt_pk_bf16_f32 v18, v18, v19
	v_cvt_pk_bf16_f32 v19, v20, v21
	v_lshlrev_b32_e32 v20, 16, v242
	v_and_b32_e32 v21, 0xffff0000, v242
	v_pk_fma_f32 v[20:21], v[30:31], s[22:23], v[20:21] op_sel_hi:[1,0,1]
	s_andn2_b64 vcc, exec, s[4:5]
	v_cvt_pk_bf16_f32 v20, v20, v21
	v_cvt_pk_bf16_f32 v21, v24, v25
	global_store_dwordx4 v[22:23], v[18:21], off offset:16
	s_mov_b64 s[4:5], -1
	s_waitcnt vmcnt(15)
	v_lshlrev_b32_e32 v18, 16, v248
	v_and_b32_e32 v19, 0xffff0000, v248
	v_pk_fma_f32 v[2:3], v[2:3], s[22:23], v[18:19] op_sel_hi:[1,0,1]
	v_lshlrev_b32_e32 v18, 16, v249
	v_and_b32_e32 v19, 0xffff0000, v249
	v_pk_fma_f32 v[4:5], v[4:5], s[22:23], v[18:19] op_sel_hi:[1,0,1]
	v_cvt_pk_bf16_f32 v2, v2, v3
	v_cvt_pk_bf16_f32 v3, v4, v5
	v_lshlrev_b32_e32 v4, 16, v250
	v_and_b32_e32 v5, 0xffff0000, v250
	v_pk_fma_f32 v[4:5], v[6:7], s[22:23], v[4:5] op_sel_hi:[1,0,1]
	v_lshlrev_b32_e32 v6, 16, v251
	v_and_b32_e32 v7, 0xffff0000, v251
	v_pk_fma_f32 v[6:7], v[8:9], s[22:23], v[6:7] op_sel_hi:[1,0,1]
	v_cvt_pk_bf16_f32 v4, v4, v5
	v_cvt_pk_bf16_f32 v5, v6, v7
	global_store_dwordx4 v[22:23], v[2:5], off offset:256
	s_waitcnt vmcnt(15)
	v_lshlrev_b32_e32 v6, 16, v217
	v_and_b32_e32 v7, 0xffff0000, v217
	v_lshlrev_b32_e32 v2, 16, v214
	v_and_b32_e32 v3, 0xffff0000, v214
	v_lshlrev_b32_e32 v4, 16, v215
	v_and_b32_e32 v5, 0xffff0000, v215
	v_pk_fma_f32 v[2:3], v[10:11], s[22:23], v[2:3] op_sel_hi:[1,0,1]
	v_pk_fma_f32 v[4:5], v[12:13], s[22:23], v[4:5] op_sel_hi:[1,0,1]
	v_cvt_pk_bf16_f32 v2, v2, v3
	v_cvt_pk_bf16_f32 v3, v4, v5
	v_lshlrev_b32_e32 v4, 16, v216
	v_and_b32_e32 v5, 0xffff0000, v216
	v_pk_fma_f32 v[4:5], v[14:15], s[22:23], v[4:5] op_sel_hi:[1,0,1]
	v_pk_fma_f32 v[6:7], v[16:17], s[22:23], v[6:7] op_sel_hi:[1,0,1]
	v_cvt_pk_bf16_f32 v4, v4, v5
	v_cvt_pk_bf16_f32 v5, v6, v7
	global_store_dwordx4 v[22:23], v[2:5], off offset:272
	s_cbranch_vccnz .LBB0_761
	s_andn2_b64 vcc, exec, s[8:9]
	s_cbranch_vccnz .LBB0_760
	s_barrier
	s_branch .LBB0_760
